# P11 (expert gate/up) epilogue rewritten by hand with packed f32 mul/fma, 32-bit store offsets; same arithmetic
# speedup vs baseline: 1.0077x; 1.0014x over previous
.LBB0_1414:
	s_lshl_b32 s2, s24, 8
	s_add_i32 s2, s2, s25
	v_and_or_b32 v145, v254, 15, s2
	s_lshl_b32 s2, s22, 7
	v_ashrrev_i32_e32 v130, 1, v254
	s_or_b32 s2, s2, s49
	v_and_b32_e32 v130, -8, v130
	v_add_u32_e32 v130, s2, v130
	v_mad_u32_u24 v246, v145, s52, v130
	v_mov_b32_e32 v250, 0xb938aa3b
	v_mov_b32_e32 v251, 0xb938aa3b
	v_mov_b32_e32 v252, 0x4b000000
	v_mov_b32_e32 v253, 0x4b000000
	v_pk_mul_f32 v[146:147], v[112:113], v[250:251]
	v_pk_mul_f32 v[148:149], v[114:115], v[250:251]
	v_pk_mul_f32 v[150:151], v[116:117], v[250:251]
	v_pk_mul_f32 v[152:153], v[118:119], v[250:251]
	v_exp_f32_e32 v146, v146
	v_exp_f32_e32 v147, v147
	v_exp_f32_e32 v148, v148
	v_exp_f32_e32 v149, v149
	v_exp_f32_e32 v150, v150
	v_exp_f32_e32 v151, v151
	v_exp_f32_e32 v152, v152
	v_exp_f32_e32 v153, v153
	v_pk_mul_f32 v[112:113], v[112:113], v[120:121]
	v_pk_mul_f32 v[114:115], v[114:115], v[122:123]
	v_pk_mul_f32 v[116:117], v[116:117], v[124:125]
	v_pk_mul_f32 v[118:119], v[118:119], v[126:127]
	v_pk_fma_f32 v[146:147], v[146:147], v[252:253], v[252:253]
	v_pk_fma_f32 v[148:149], v[148:149], v[252:253], v[252:253]
	v_pk_fma_f32 v[150:151], v[150:151], v[252:253], v[252:253]
	v_pk_fma_f32 v[152:153], v[152:153], v[252:253], v[252:253]
	v_rcp_f32_e32 v146, v146
	v_rcp_f32_e32 v147, v147
	v_rcp_f32_e32 v148, v148
	v_rcp_f32_e32 v149, v149
	v_rcp_f32_e32 v150, v150
	v_rcp_f32_e32 v151, v151
	v_rcp_f32_e32 v152, v152
	v_rcp_f32_e32 v153, v153
	v_mov_b32_e32 v156, v246
	v_pk_mul_f32 v[112:113], v[112:113], v[146:147]
	v_pk_mul_f32 v[114:115], v[114:115], v[148:149]
	v_pk_mul_f32 v[116:117], v[116:117], v[150:151]
	v_pk_mul_f32 v[118:119], v[118:119], v[152:153]
	v_med3_f32 v112, v112, s51, v144
	v_med3_f32 v113, v113, s51, v144
	v_med3_f32 v114, v114, s51, v144
	v_med3_f32 v115, v115, s51, v144
	v_med3_f32 v116, v116, s51, v144
	v_med3_f32 v117, v117, s51, v144
	v_med3_f32 v118, v118, s51, v144
	v_med3_f32 v119, v119, s51, v144
	v_cvt_pk_fp8_f32 v154, v112, v113
	v_cvt_pk_fp8_f32 v155, v116, v117
	v_cvt_pk_fp8_f32 v154, v114, v115 op_sel:[0,0,1]
	v_cvt_pk_fp8_f32 v155, v118, v119 op_sel:[0,0,1]
	s_nop 0
	global_store_dwordx2 v156, v[154:155], s[10:11]
	v_pk_mul_f32 v[160:161], v[100:101], v[250:251]
	v_pk_mul_f32 v[162:163], v[102:103], v[250:251]
	v_pk_mul_f32 v[164:165], v[96:97], v[250:251]
	v_pk_mul_f32 v[166:167], v[98:99], v[250:251]
	v_exp_f32_e32 v160, v160
	v_exp_f32_e32 v161, v161
	v_exp_f32_e32 v162, v162
	v_exp_f32_e32 v163, v163
	v_exp_f32_e32 v164, v164
	v_exp_f32_e32 v165, v165
	v_exp_f32_e32 v166, v166
	v_exp_f32_e32 v167, v167
	v_pk_mul_f32 v[100:101], v[100:101], v[108:109]
	v_pk_mul_f32 v[102:103], v[102:103], v[110:111]
	v_pk_mul_f32 v[96:97], v[96:97], v[104:105]
	v_pk_mul_f32 v[98:99], v[98:99], v[106:107]
	v_pk_fma_f32 v[160:161], v[160:161], v[252:253], v[252:253]
	v_pk_fma_f32 v[162:163], v[162:163], v[252:253], v[252:253]
	v_pk_fma_f32 v[164:165], v[164:165], v[252:253], v[252:253]
	v_pk_fma_f32 v[166:167], v[166:167], v[252:253], v[252:253]
	v_rcp_f32_e32 v160, v160
	v_rcp_f32_e32 v161, v161
	v_rcp_f32_e32 v162, v162
	v_rcp_f32_e32 v163, v163
	v_rcp_f32_e32 v164, v164
	v_rcp_f32_e32 v165, v165
	v_rcp_f32_e32 v166, v166
	v_rcp_f32_e32 v167, v167
	v_add_u32_e32 v170, 0x1c000, v246
	v_pk_mul_f32 v[100:101], v[100:101], v[160:161]
	v_pk_mul_f32 v[102:103], v[102:103], v[162:163]
	v_pk_mul_f32 v[96:97], v[96:97], v[164:165]
	v_pk_mul_f32 v[98:99], v[98:99], v[166:167]
	v_med3_f32 v100, v100, s51, v144
	v_med3_f32 v101, v101, s51, v144
	v_med3_f32 v102, v102, s51, v144
	v_med3_f32 v103, v103, s51, v144
	v_med3_f32 v96, v96, s51, v144
	v_med3_f32 v97, v97, s51, v144
	v_med3_f32 v98, v98, s51, v144
	v_med3_f32 v99, v99, s51, v144
	v_cvt_pk_fp8_f32 v168, v100, v101
	v_cvt_pk_fp8_f32 v169, v96, v97
	v_cvt_pk_fp8_f32 v168, v102, v103 op_sel:[0,0,1]
	v_cvt_pk_fp8_f32 v169, v98, v99 op_sel:[0,0,1]
	s_nop 0
	global_store_dwordx2 v170, v[168:169], s[10:11]
	v_pk_mul_f32 v[146:147], v[84:85], v[250:251]
	v_pk_mul_f32 v[148:149], v[86:87], v[250:251]
	v_pk_mul_f32 v[150:151], v[80:81], v[250:251]
	v_pk_mul_f32 v[152:153], v[82:83], v[250:251]
	v_exp_f32_e32 v146, v146
	v_exp_f32_e32 v147, v147
	v_exp_f32_e32 v148, v148
	v_exp_f32_e32 v149, v149
	v_exp_f32_e32 v150, v150
	v_exp_f32_e32 v151, v151
	v_exp_f32_e32 v152, v152
	v_exp_f32_e32 v153, v153
	v_pk_mul_f32 v[84:85], v[84:85], v[92:93]
	v_pk_mul_f32 v[86:87], v[86:87], v[94:95]
	v_pk_mul_f32 v[80:81], v[80:81], v[88:89]
	v_pk_mul_f32 v[82:83], v[82:83], v[90:91]
	v_pk_fma_f32 v[146:147], v[146:147], v[252:253], v[252:253]
	v_pk_fma_f32 v[148:149], v[148:149], v[252:253], v[252:253]
	v_pk_fma_f32 v[150:151], v[150:151], v[252:253], v[252:253]
	v_pk_fma_f32 v[152:153], v[152:153], v[252:253], v[252:253]
	v_rcp_f32_e32 v146, v146
	v_rcp_f32_e32 v147, v147
	v_rcp_f32_e32 v148, v148
	v_rcp_f32_e32 v149, v149
	v_rcp_f32_e32 v150, v150
	v_rcp_f32_e32 v151, v151
	v_rcp_f32_e32 v152, v152
	v_rcp_f32_e32 v153, v153
	v_add_u32_e32 v156, 0x38000, v246
	v_pk_mul_f32 v[84:85], v[84:85], v[146:147]
	v_pk_mul_f32 v[86:87], v[86:87], v[148:149]
	v_pk_mul_f32 v[80:81], v[80:81], v[150:151]
	v_pk_mul_f32 v[82:83], v[82:83], v[152:153]
	v_med3_f32 v84, v84, s51, v144
	v_med3_f32 v85, v85, s51, v144
	v_med3_f32 v86, v86, s51, v144
	v_med3_f32 v87, v87, s51, v144
	v_med3_f32 v80, v80, s51, v144
	v_med3_f32 v81, v81, s51, v144
	v_med3_f32 v82, v82, s51, v144
	v_med3_f32 v83, v83, s51, v144
	v_cvt_pk_fp8_f32 v154, v84, v85
	v_cvt_pk_fp8_f32 v155, v80, v81
	v_cvt_pk_fp8_f32 v154, v86, v87 op_sel:[0,0,1]
	v_cvt_pk_fp8_f32 v155, v82, v83 op_sel:[0,0,1]
	s_nop 0
	global_store_dwordx2 v156, v[154:155], s[10:11]
	v_pk_mul_f32 v[160:161], v[60:61], v[250:251]
	v_pk_mul_f32 v[162:163], v[62:63], v[250:251]
	v_pk_mul_f32 v[164:165], v[56:57], v[250:251]
	v_pk_mul_f32 v[166:167], v[58:59], v[250:251]
	v_exp_f32_e32 v160, v160
	v_exp_f32_e32 v161, v161
	v_exp_f32_e32 v162, v162
	v_exp_f32_e32 v163, v163
	v_exp_f32_e32 v164, v164
	v_exp_f32_e32 v165, v165
	v_exp_f32_e32 v166, v166
	v_exp_f32_e32 v167, v167
	v_pk_mul_f32 v[60:61], v[60:61], v[76:77]
	v_pk_mul_f32 v[62:63], v[62:63], v[78:79]
	v_pk_mul_f32 v[56:57], v[56:57], v[72:73]
	v_pk_mul_f32 v[58:59], v[58:59], v[74:75]
	v_pk_fma_f32 v[160:161], v[160:161], v[252:253], v[252:253]
	v_pk_fma_f32 v[162:163], v[162:163], v[252:253], v[252:253]
	v_pk_fma_f32 v[164:165], v[164:165], v[252:253], v[252:253]
	v_pk_fma_f32 v[166:167], v[166:167], v[252:253], v[252:253]
	v_rcp_f32_e32 v160, v160
	v_rcp_f32_e32 v161, v161
	v_rcp_f32_e32 v162, v162
	v_rcp_f32_e32 v163, v163
	v_rcp_f32_e32 v164, v164
	v_rcp_f32_e32 v165, v165
	v_rcp_f32_e32 v166, v166
	v_rcp_f32_e32 v167, v167
	v_add_u32_e32 v170, 0x54000, v246
	v_pk_mul_f32 v[60:61], v[60:61], v[160:161]
	v_pk_mul_f32 v[62:63], v[62:63], v[162:163]
	v_pk_mul_f32 v[56:57], v[56:57], v[164:165]
	v_pk_mul_f32 v[58:59], v[58:59], v[166:167]
	v_med3_f32 v60, v60, s51, v144
	v_med3_f32 v61, v61, s51, v144
	v_med3_f32 v62, v62, s51, v144
	v_med3_f32 v63, v63, s51, v144
	v_med3_f32 v56, v56, s51, v144
	v_med3_f32 v57, v57, s51, v144
	v_med3_f32 v58, v58, s51, v144
	v_med3_f32 v59, v59, s51, v144
	v_cvt_pk_fp8_f32 v168, v60, v61
	v_cvt_pk_fp8_f32 v169, v56, v57
	v_cvt_pk_fp8_f32 v168, v62, v63 op_sel:[0,0,1]
	v_cvt_pk_fp8_f32 v169, v58, v59 op_sel:[0,0,1]
	s_nop 0
	global_store_dwordx2 v170, v[168:169], s[10:11]
	v_pk_mul_f32 v[146:147], v[52:53], v[250:251]
	v_pk_mul_f32 v[148:149], v[54:55], v[250:251]
	v_pk_mul_f32 v[150:151], v[48:49], v[250:251]
	v_pk_mul_f32 v[152:153], v[50:51], v[250:251]
	v_exp_f32_e32 v146, v146
	v_exp_f32_e32 v147, v147
	v_exp_f32_e32 v148, v148
	v_exp_f32_e32 v149, v149
	v_exp_f32_e32 v150, v150
	v_exp_f32_e32 v151, v151
	v_exp_f32_e32 v152, v152
	v_exp_f32_e32 v153, v153
	v_pk_mul_f32 v[52:53], v[52:53], v[68:69]
	v_pk_mul_f32 v[54:55], v[54:55], v[70:71]
	v_pk_mul_f32 v[48:49], v[48:49], v[64:65]
	v_pk_mul_f32 v[50:51], v[50:51], v[66:67]
	v_pk_fma_f32 v[146:147], v[146:147], v[252:253], v[252:253]
	v_pk_fma_f32 v[148:149], v[148:149], v[252:253], v[252:253]
	v_pk_fma_f32 v[150:151], v[150:151], v[252:253], v[252:253]
	v_pk_fma_f32 v[152:153], v[152:153], v[252:253], v[252:253]
	v_rcp_f32_e32 v146, v146
	v_rcp_f32_e32 v147, v147
	v_rcp_f32_e32 v148, v148
	v_rcp_f32_e32 v149, v149
	v_rcp_f32_e32 v150, v150
	v_rcp_f32_e32 v151, v151
	v_rcp_f32_e32 v152, v152
	v_rcp_f32_e32 v153, v153
	v_add_u32_e32 v156, 0xe0000, v246
	v_pk_mul_f32 v[52:53], v[52:53], v[146:147]
	v_pk_mul_f32 v[54:55], v[54:55], v[148:149]
	v_pk_mul_f32 v[48:49], v[48:49], v[150:151]
	v_pk_mul_f32 v[50:51], v[50:51], v[152:153]
	v_med3_f32 v52, v52, s51, v144
	v_med3_f32 v53, v53, s51, v144
	v_med3_f32 v54, v54, s51, v144
	v_med3_f32 v55, v55, s51, v144
	v_med3_f32 v48, v48, s51, v144
	v_med3_f32 v49, v49, s51, v144
	v_med3_f32 v50, v50, s51, v144
	v_med3_f32 v51, v51, s51, v144
	v_cvt_pk_fp8_f32 v154, v52, v53
	v_cvt_pk_fp8_f32 v155, v48, v49
	v_cvt_pk_fp8_f32 v154, v54, v55 op_sel:[0,0,1]
	v_cvt_pk_fp8_f32 v155, v50, v51 op_sel:[0,0,1]
	s_nop 0
	global_store_dwordx2 v156, v[154:155], s[10:11]
	v_pk_mul_f32 v[160:161], v[36:37], v[250:251]
	v_pk_mul_f32 v[162:163], v[38:39], v[250:251]
	v_pk_mul_f32 v[164:165], v[32:33], v[250:251]
	v_pk_mul_f32 v[166:167], v[34:35], v[250:251]
	v_exp_f32_e32 v160, v160
	v_exp_f32_e32 v161, v161
	v_exp_f32_e32 v162, v162
	v_exp_f32_e32 v163, v163
	v_exp_f32_e32 v164, v164
	v_exp_f32_e32 v165, v165
	v_exp_f32_e32 v166, v166
	v_exp_f32_e32 v167, v167
	v_pk_mul_f32 v[36:37], v[36:37], v[44:45]
	v_pk_mul_f32 v[38:39], v[38:39], v[46:47]
	v_pk_mul_f32 v[32:33], v[32:33], v[40:41]
	v_pk_mul_f32 v[34:35], v[34:35], v[42:43]
	v_pk_fma_f32 v[160:161], v[160:161], v[252:253], v[252:253]
	v_pk_fma_f32 v[162:163], v[162:163], v[252:253], v[252:253]
	v_pk_fma_f32 v[164:165], v[164:165], v[252:253], v[252:253]
	v_pk_fma_f32 v[166:167], v[166:167], v[252:253], v[252:253]
	v_rcp_f32_e32 v160, v160
	v_rcp_f32_e32 v161, v161
	v_rcp_f32_e32 v162, v162
	v_rcp_f32_e32 v163, v163
	v_rcp_f32_e32 v164, v164
	v_rcp_f32_e32 v165, v165
	v_rcp_f32_e32 v166, v166
	v_rcp_f32_e32 v167, v167
	v_add_u32_e32 v170, 0xfc000, v246
	v_pk_mul_f32 v[36:37], v[36:37], v[160:161]
	v_pk_mul_f32 v[38:39], v[38:39], v[162:163]
	v_pk_mul_f32 v[32:33], v[32:33], v[164:165]
	v_pk_mul_f32 v[34:35], v[34:35], v[166:167]
	v_med3_f32 v36, v36, s51, v144
	v_med3_f32 v37, v37, s51, v144
	v_med3_f32 v38, v38, s51, v144
	v_med3_f32 v39, v39, s51, v144
	v_med3_f32 v32, v32, s51, v144
	v_med3_f32 v33, v33, s51, v144
	v_med3_f32 v34, v34, s51, v144
	v_med3_f32 v35, v35, s51, v144
	v_cvt_pk_fp8_f32 v168, v36, v37
	v_cvt_pk_fp8_f32 v169, v32, v33
	v_cvt_pk_fp8_f32 v168, v38, v39 op_sel:[0,0,1]
	v_cvt_pk_fp8_f32 v169, v34, v35 op_sel:[0,0,1]
	s_nop 0
	global_store_dwordx2 v170, v[168:169], s[10:11]
	v_pk_mul_f32 v[146:147], v[20:21], v[250:251]
	v_pk_mul_f32 v[148:149], v[22:23], v[250:251]
	v_pk_mul_f32 v[150:151], v[16:17], v[250:251]
	v_pk_mul_f32 v[152:153], v[18:19], v[250:251]
	v_exp_f32_e32 v146, v146
	v_exp_f32_e32 v147, v147
	v_exp_f32_e32 v148, v148
	v_exp_f32_e32 v149, v149
	v_exp_f32_e32 v150, v150
	v_exp_f32_e32 v151, v151
	v_exp_f32_e32 v152, v152
	v_exp_f32_e32 v153, v153
	v_pk_mul_f32 v[20:21], v[20:21], v[28:29]
	v_pk_mul_f32 v[22:23], v[22:23], v[30:31]
	v_pk_mul_f32 v[16:17], v[16:17], v[24:25]
	v_pk_mul_f32 v[18:19], v[18:19], v[26:27]
	v_pk_fma_f32 v[146:147], v[146:147], v[252:253], v[252:253]
	v_pk_fma_f32 v[148:149], v[148:149], v[252:253], v[252:253]
	v_pk_fma_f32 v[150:151], v[150:151], v[252:253], v[252:253]
	v_pk_fma_f32 v[152:153], v[152:153], v[252:253], v[252:253]
	v_rcp_f32_e32 v146, v146
	v_rcp_f32_e32 v147, v147
	v_rcp_f32_e32 v148, v148
	v_rcp_f32_e32 v149, v149
	v_rcp_f32_e32 v150, v150
	v_rcp_f32_e32 v151, v151
	v_rcp_f32_e32 v152, v152
	v_rcp_f32_e32 v153, v153
	v_add_u32_e32 v156, 0x118000, v246
	v_pk_mul_f32 v[20:21], v[20:21], v[146:147]
	v_pk_mul_f32 v[22:23], v[22:23], v[148:149]
	v_pk_mul_f32 v[16:17], v[16:17], v[150:151]
	v_pk_mul_f32 v[18:19], v[18:19], v[152:153]
	v_med3_f32 v20, v20, s51, v144
	v_med3_f32 v21, v21, s51, v144
	v_med3_f32 v22, v22, s51, v144
	v_med3_f32 v23, v23, s51, v144
	v_med3_f32 v16, v16, s51, v144
	v_med3_f32 v17, v17, s51, v144
	v_med3_f32 v18, v18, s51, v144
	v_med3_f32 v19, v19, s51, v144
	v_cvt_pk_fp8_f32 v154, v20, v21
	v_cvt_pk_fp8_f32 v155, v16, v17
	v_cvt_pk_fp8_f32 v154, v22, v23 op_sel:[0,0,1]
	v_cvt_pk_fp8_f32 v155, v18, v19 op_sel:[0,0,1]
	s_nop 0
	global_store_dwordx2 v156, v[154:155], s[10:11]
	v_pk_mul_f32 v[160:161], v[4:5], v[250:251]
	v_pk_mul_f32 v[162:163], v[6:7], v[250:251]
	v_pk_mul_f32 v[164:165], v[0:1], v[250:251]
	v_pk_mul_f32 v[166:167], v[2:3], v[250:251]
	v_exp_f32_e32 v160, v160
	v_exp_f32_e32 v161, v161
	v_exp_f32_e32 v162, v162
	v_exp_f32_e32 v163, v163
	v_exp_f32_e32 v164, v164
	v_exp_f32_e32 v165, v165
	v_exp_f32_e32 v166, v166
	v_exp_f32_e32 v167, v167
	v_pk_mul_f32 v[4:5], v[4:5], v[12:13]
	v_pk_mul_f32 v[6:7], v[6:7], v[14:15]
	v_pk_mul_f32 v[0:1], v[0:1], v[8:9]
	v_pk_mul_f32 v[2:3], v[2:3], v[10:11]
	v_pk_fma_f32 v[160:161], v[160:161], v[252:253], v[252:253]
	v_pk_fma_f32 v[162:163], v[162:163], v[252:253], v[252:253]
	v_pk_fma_f32 v[164:165], v[164:165], v[252:253], v[252:253]
	v_pk_fma_f32 v[166:167], v[166:167], v[252:253], v[252:253]
	v_rcp_f32_e32 v160, v160
	v_rcp_f32_e32 v161, v161
	v_rcp_f32_e32 v162, v162
	v_rcp_f32_e32 v163, v163
	v_rcp_f32_e32 v164, v164
	v_rcp_f32_e32 v165, v165
	v_rcp_f32_e32 v166, v166
	v_rcp_f32_e32 v167, v167
	v_add_u32_e32 v170, 0x134000, v246
	v_pk_mul_f32 v[4:5], v[4:5], v[160:161]
	v_pk_mul_f32 v[6:7], v[6:7], v[162:163]
	v_pk_mul_f32 v[0:1], v[0:1], v[164:165]
	v_pk_mul_f32 v[2:3], v[2:3], v[166:167]
	v_med3_f32 v4, v4, s51, v144
	v_med3_f32 v5, v5, s51, v144
	v_med3_f32 v6, v6, s51, v144
	v_med3_f32 v7, v7, s51, v144
	v_med3_f32 v0, v0, s51, v144
	v_med3_f32 v1, v1, s51, v144
	v_med3_f32 v2, v2, s51, v144
	v_med3_f32 v3, v3, s51, v144
	v_cvt_pk_fp8_f32 v168, v4, v5
	v_cvt_pk_fp8_f32 v169, v0, v1
	v_cvt_pk_fp8_f32 v168, v6, v7 op_sel:[0,0,1]
	v_cvt_pk_fp8_f32 v169, v2, v3 op_sel:[0,0,1]
	s_nop 0
	global_store_dwordx2 v170, v[168:169], s[10:11]
	s_and_b64 vcc, exec, s[4:5]
	s_mov_b64 s[4:5], -1
	s_cbranch_vccnz .LBB0_1403
	s_andn2_b64 vcc, exec, s[8:9]
	s_cbranch_vccnz .LBB0_1402
	s_barrier
	s_branch .LBB0_1402
